# v29 + original grid barrier code, XCD-local shortcut (no L2 writeback, no top-level round) at the seams out-proj->logits, logits->xattn-out, mlp1->mlp2
# speedup vs baseline: 1.0033x; 1.0033x over previous
.LBB0_1389:
	s_andn2_saveexec_b64 s[8:9], s[22:23]
	s_cbranch_execz .LBB0_1409
	s_mov_b64 s[22:23], exec
	s_branch .LBB0_1406
	buffer_wbl2 sc1
	s_waitcnt lgkmcnt(0)
	s_waitcnt vmcnt(0)
	v_mbcnt_lo_u32_b32 v1, s22, 0
	v_mbcnt_hi_u32_b32 v1, s23, v1
	v_cmp_eq_u32_e32 vcc, 0, v1
	s_and_saveexec_b64 s[26:27], vcc
	s_cbranch_execz .LBB0_1392
	s_bcnt1_i32_b64 s1, s[22:23]
	v_readlane_b32 s8, v253, 49
	v_mov_b32_e32 v2, s1
	v_readlane_b32 s9, v253, 50
	s_nop 4
	global_atomic_add v2, v129, v2, s[8:9] sc0

.LBB0_1731:
	s_andn2_saveexec_b64 s[8:9], s[30:31]
	s_cbranch_execz .LBB0_1751
	s_mov_b64 s[30:31], exec
	s_branch .LBB0_1748
	buffer_wbl2 sc1
	s_waitcnt lgkmcnt(0)
	s_waitcnt vmcnt(0)
	v_mbcnt_lo_u32_b32 v1, s30, 0
	v_mbcnt_hi_u32_b32 v1, s31, v1
	v_cmp_eq_u32_e32 vcc, 0, v1
	s_and_saveexec_b64 s[38:39], vcc
	s_cbranch_execz .LBB0_1734
	s_bcnt1_i32_b64 s1, s[30:31]
	v_readlane_b32 s8, v253, 49
	v_mov_b32_e32 v2, s1
	v_readlane_b32 s9, v253, 50
	s_nop 4
	global_atomic_add v2, v129, v2, s[8:9] sc0
